# attention phase: attention-first waves (behind the barrier) take 4 copy items, copy-first waves 8 (was 6 each)
# speedup vs baseline: 1.0070x; 1.0030x over previous
; #define LAS __attribute__((address_space(3)))
; __global__ void __launch_bounds__(512, 2) hymba_fwd(Args args) {
;     ...
;         LAS unsigned char* vbuf = lds + wave * 12288;
;         {
;             constexpr int CV_LO = CV_N1, CV_HI = CV_GU + CV_D - CV_N5, CV_EXP = CV_HI - CV_LO;
;             const int nA = (512 - bx + G - 1) / G;
;             const int per_wave = (CV_EXP + NGW - 1) / NGW;
;             const int c_lo = CV_LO + gw * per_wave, c_hi = (c_lo + per_wave < CV_HI) ? c_lo + per_wave : CV_HI;
;             const int nsteps = nA > 0 ? nA : 1, per_batch = (per_wave + nsteps - 1) / nsteps;
;             int ia = 0, ic = c_lo;
; #pragma unroll 1
;             for (int hs = 0; hs < 2 * nsteps; ++hs) {
;                 const bool doA = (((hs & 1) == 0) == (wave < 4));
.LBB0_212:
	s_or_b64 exec, exec, s[0:1]
	s_abs_i32 s0, s3
	v_cvt_f32_u32_e32 v1, s0
	s_mul_i32 s1, s92, 0x3000
	s_add_i32 s68, s1, 0
	s_sub_i32 s1, s3, s2
	v_rcp_iflag_f32_e32 v1, v1
	s_add_i32 s6, s1, 0x1ff
	s_sub_i32 s1, 0xfffffe01, s1
	s_xor_b32 s7, s6, s3
	v_mul_f32_e32 v1, 0x4f7ffffe, v1
	v_cvt_u32_f32_e32 v1, v1
	s_max_i32 s1, s6, s1
	s_sub_i32 s6, 0, s0
	s_ashr_i32 s7, s7, 31
	v_readfirstlane_b32 s20, v1
	s_mul_i32 s6, s6, s20
	s_mul_hi_u32 s6, s20, s6
	s_add_i32 s20, s20, s6
	s_mul_hi_u32 s6, s1, s20
	s_mul_i32 s20, s6, s0
	s_sub_i32 s1, s1, s20
	s_add_i32 s20, s6, 1
	s_sub_i32 s21, s1, s0
	s_cmp_ge_u32 s1, s0
	s_cselect_b32 s6, s20, s6
	s_cselect_b32 s1, s21, s1
	s_add_i32 s20, s6, 1
	s_cmp_ge_u32 s1, s0
	s_cselect_b32 s0, s20, s6
	s_abs_i32 s6, s90
	v_cvt_f32_u32_e32 v1, s6
	s_sub_i32 s20, 0, s6
	s_xor_b32 s0, s0, s7
	s_sub_i32 s69, s0, s7
	v_rcp_iflag_f32_e32 v1, v1
	s_add_i32 s0, s90, 0x2fff
	s_xor_b32 s7, s0, s90
	s_abs_i32 s0, s0
	v_mul_f32_e32 v1, 0x4f7ffffe, v1
	v_cvt_u32_f32_e32 v1, v1
	s_ashr_i32 s7, s7, 31
	v_lshlrev_b32_e32 v4, 1, v159
	v_lshrrev_b32_e32 v3, 2, v159
	v_readfirstlane_b32 s21, v1
	s_mul_i32 s20, s20, s21
	s_mul_hi_u32 s20, s21, s20
	s_add_i32 s21, s21, s20
	s_mul_hi_u32 s20, s0, s21
	s_mul_i32 s21, s20, s6
	s_sub_i32 s0, s0, s21
	s_add_i32 s21, s20, 1
	s_sub_i32 s22, s0, s6
	s_cmp_ge_u32 s0, s6
	s_cselect_b32 s20, s21, s20
	s_cselect_b32 s0, s22, s0
	s_add_i32 s21, s20, 1
	s_cmp_ge_u32 s0, s6
	s_cselect_b32 s0, s21, s20
	s_max_i32 s6, s69, 1
	v_cvt_f32_u32_e32 v1, s6
	s_xor_b32 s0, s0, s7
	s_sub_i32 s0, s0, s7
	s_mul_i32 s7, s0, s34
	v_rcp_iflag_f32_e32 v1, v1
	v_and_b32_e32 v4, 32, v4
	s_add_i32 s67, s7, 0x7800
	s_sub_i32 s20, 0, s6
	v_mul_f32_e32 v1, 0x4f7ffffe, v1
	v_cvt_u32_f32_e32 v1, v1
	s_mul_i32 s100, s92, 2
	s_sub_i32 s101, s100, 16
	s_sub_i32 s100, 0, s100
	s_cmp_lt_u32 s92, 4
	s_cselect_b32 s100, s100, s101
	s_cselect_b32 s101, -2, 2
	s_add_i32 s67, s67, s100
	s_add_i32 s0, s0, s101
	s_add_i32 s7, s67, s0
	s_add_i32 s0, s6, s0
	s_add_i32 s0, s0, -1
	v_readfirstlane_b32 s21, v1
	v_lshlrev_b32_e32 v1, 3, v159
	v_and_b32_e32 v2, 0x1c0, v1
	v_add_u32_e32 v163, s68, v2
	v_and_b32_e32 v165, 56, v1
	v_bfe_u32 v2, v0, 2, 2
	v_and_b32_e32 v1, 24, v1
	v_add3_u32 v167, s68, v4, v1
	v_and_or_b32 v1, v3, 8, v2
	s_mul_i32 s20, s20, s21
	v_lshlrev_b32_e32 v169, 6, v1
	v_lshlrev_b32_e32 v1, 8, v159
	s_mul_hi_u32 s20, s21, s20
	v_and_b32_e32 v1, 0x1f00, v1
	v_lshrrev_b32_e32 v2, 5, v159
	s_min_i32 s66, s7, 0xa800
	s_ashr_i32 s7, s0, 31
	s_abs_i32 s0, s0
	s_add_i32 s21, s21, s20
	v_add_u32_e32 v204, s68, v1
	v_and_b32_e32 v1, 15, v0
	v_bitop3_b32 v3, v2, v0, 15 bitop3:0x78
	s_mul_hi_u32 s20, s0, s21
	v_lshlrev_b32_e32 v205, 4, v3
	v_bitop3_b32 v3, v2, v1, 2 bitop3:0x36
	s_mul_i32 s21, s20, s6
	v_lshlrev_b32_e32 v206, 4, v3
	v_bitop3_b32 v3, v2, v1, 4 bitop3:0x36
	s_sub_i32 s0, s0, s21
	v_lshlrev_b32_e32 v207, 4, v3
	v_bitop3_b32 v3, v2, v1, 6 bitop3:0x36
	s_add_i32 s21, s20, 1
	s_sub_i32 s22, s0, s6
	v_lshlrev_b32_e32 v208, 4, v3
	v_bitop3_b32 v3, v2, v1, 8 bitop3:0x36
	s_cmp_ge_u32 s0, s6
	v_lshlrev_b32_e32 v209, 4, v3
	v_bitop3_b32 v3, v2, v1, 10 bitop3:0x36
	s_cselect_b32 s20, s21, s20
	v_lshlrev_b32_e32 v210, 4, v3
	v_bitop3_b32 v3, v2, v1, 12 bitop3:0x36
	v_bitop3_b32 v1, v2, v1, 14 bitop3:0x36
	v_and_b32_e32 v0, 7, v0
	s_cselect_b32 s0, s22, s0
	s_add_i32 s21, s20, 1
	v_lshrrev_b32_e32 v158, 3, v159
	v_lshlrev_b32_e32 v212, 4, v1
	v_lshlrev_b32_e32 v1, 1, v0
	s_cmp_ge_u32 s0, s6
	v_lshlrev_b32_e32 v160, 4, v0
	v_xor_b32_e32 v0, v158, v1
	s_cselect_b32 s0, s21, s20
	v_lshlrev_b32_e32 v214, 4, v0
	v_bitop3_b32 v0, v1, v158, 1 bitop3:0x36
	s_xor_b32 s0, s0, s7
	v_or_b32_e32 v2, 1, v1
	v_lshlrev_b32_e32 v215, 4, v0
	v_bitop3_b32 v0, v158, v1, 8 bitop3:0x36
	s_sub_i32 s72, s0, s7
	s_lshl_b32 s73, s6, 1
	v_lshlrev_b32_e32 v217, 4, v0
	v_bitop3_b32 v0, v158, v2, 8 bitop3:0x36
	v_or_b32_e32 v166, 24, v158
	s_cmpk_gt_u32 s74, 0xff
	v_lshlrev_b32_e32 v218, 4, v0
	v_bitop3_b32 v0, v166, v1, 15 bitop3:0x6c
	v_mov_b32_e32 v171, 0
	v_or_b32_e32 v162, 8, v158
	v_or_b32_e32 v164, 16, v158
	v_lshlrev_b32_e32 v221, 4, v0
	v_bitop3_b32 v0, v166, v2, 15 bitop3:0x6c
	s_cselect_b64 s[6:7], -1, 0
	s_mov_b32 s20, 0x3f803f80
	s_mov_b32 s1, 0
	s_mov_b32 s96, s74
	v_and_b32_e32 v168, 28, v157
	v_lshlrev_b32_e32 v211, 4, v3
	v_mov_b32_e32 v161, v171
	v_lshl_add_u32 v213, v158, 8, s68
	v_lshl_add_u32 v216, v162, 8, s68
	v_lshl_add_u32 v219, v164, 8, s68
	v_lshl_add_u32 v220, v166, 8, s68
	v_lshlrev_b32_e32 v222, 4, v0
	v_cndmask_b32_e64 v223, 0, 1, s[6:7]
	s_movk_i32 s74, 0x60
	s_add_i32 s75, 0, 0x180b4
	s_mov_b32 s76, 0x5fc0000
	s_mov_b32 s77, 0x6fc0000
	s_mov_b32 s78, 0x5fd0000
	s_mov_b32 s79, 0x6fd0000
	s_mov_b32 s80, 0x5fe0000
	s_mov_b32 s81, 0x6fe0000
	s_mov_b32 s40, 0x3f803f80
	s_mov_b32 s41, s20
	s_mov_b32 s42, s20
	s_mov_b32 s43, s20
	v_mov_b32_e32 v0, 0x3f803f80
	s_mov_b32 s82, 0
	s_mov_b32 s83, 0
	s_waitcnt lgkmcnt(0)
	s_barrier
	s_branch .LBB0_214
